# grid barrier rewritten: group (blockIdx&7) returning arrive add; last of group adds to 8 release replicas; all poll own-XCD replica; all stores sc1; no wbl2; early inv
# speedup vs baseline: 1.0347x; 1.0192x over previous
.LBB0_8:
	s_or_b64 exec, exec, s[0:1]
	s_waitcnt lgkmcnt(0)
	s_barrier
	s_add_u32 s84, s54, 0x4000
	s_getreg_b32 s0, hwreg(HW_REG_XCC_ID, 0, 4)
	s_addc_u32 s85, s55, 0
	s_and_b32 s86, s0, 15
	s_and_b32 s99, s86, 7
	s_lshl_b32 s99, s99, 8
	s_add_u32 s99, s99, 0x800
	s_lshl_b32 s99, s99, 16
	s_and_b32 s98, s89, 7
	s_lshl_b32 s98, s98, 8
	s_or_b32 s99, s99, s98
	s_add_u32 s100, s54, 0x8000
	s_addc_u32 s101, s55, 0
	s_mov_b32 s98, s33
	v_cmp_ne_u32_e64 s[0:1], 0, v0
	v_cmp_eq_u32_e64 s[78:79], 0, v0
	s_nop 0
	v_writelane_b32 v253, s0, 34
	s_nop 1
	v_writelane_b32 v253, s1, 35
	s_and_saveexec_b64 s[0:1], s[78:79]
	s_cbranch_execz .LBB0_11
	s_mov_b64 s[4:5], exec
	v_mbcnt_lo_u32_b32 v1, s4, 0
	v_mbcnt_hi_u32_b32 v1, s5, v1
	v_cmp_eq_u32_e32 vcc, 0, v1
	s_and_b64 s[2:3], exec, vcc
	s_mov_b64 exec, s[2:3]
	s_cbranch_execz .LBB0_11
	s_lshl_b32 s2, s86, 8
	s_bcnt1_i32_b64 s3, s[4:5]
	v_mov_b32_e32 v1, s2
	v_mov_b32_e32 v2, s3
	global_atomic_add v1, v2, s[84:85] offset:1024

.LBB0_230:
	v_writelane_b32 v253, s40, 46
	s_cmp_gt_i32 s81, 1
	s_cselect_b64 s[4:5], -1, 0
	v_writelane_b32 v253, s41, 47
	v_writelane_b32 v253, s42, 48
	v_writelane_b32 v253, s43, 49
	v_writelane_b32 v253, s44, 50
	v_writelane_b32 v253, s45, 51
	v_writelane_b32 v253, s46, 52
	v_writelane_b32 v253, s47, 53
	v_writelane_b32 v253, s48, 54
	v_writelane_b32 v253, s49, 55
	v_writelane_b32 v253, s50, 56
	v_writelane_b32 v253, s51, 57
	v_writelane_b32 v253, s52, 58
	v_writelane_b32 v253, s53, 59
	s_and_b64 s[0:1], s[0:1], s[4:5]
	v_writelane_b32 v253, s54, 60
	s_andn2_b64 vcc, exec, s[0:1]
	v_writelane_b32 v253, s55, 61
	s_cbranch_vccnz .LBB0_284
	s_waitcnt vmcnt(0)
	s_barrier
	s_and_saveexec_b64 s[0:1], s[78:79]
	s_cbranch_execz .LBB0_283
	v_mov_b32_e32 v1, 0x22160
	s_waitcnt vmcnt(0) lgkmcnt(0)
	ds_read_b32 v2, v1
	v_mov_b32_e32 v3, 1
	v_mov_b32_e32 v4, s99
	v_and_b32_e32 v5, 0xffff, v4
	v_lshrrev_b32_e32 v6, 16, v4
	global_atomic_add v7, v5, v3, s[100:101] sc0
	buffer_inv sc1
	v_lshrrev_b32_e32 v8, 8, v5
	v_sub_u32_e32 v8, s98, v8
	v_add_u32_e32 v8, 7, v8
	v_lshrrev_b32_e32 v8, 3, v8
	v_mov_b32_e32 v9, s98
	v_min_u32_e32 v9, 8, v9
	v_mov_b32_e32 v10, 0
	s_waitcnt lgkmcnt(0)
	v_add_u32_e32 v2, 1, v2
	ds_write_b32 v1, v2
	v_mul_lo_u32 v8, v8, v2
	v_mul_lo_u32 v9, v9, v2
	s_waitcnt vmcnt(0)
	v_add_u32_e32 v7, 1, v7
	v_cmp_eq_u32_e32 vcc, v7, v8
	s_cbranch_vccz .Lgb_poll_0
	v_mov_b32_e32 v4, 0
	global_atomic_add v4, v3, s[100:101] offset:2048
	global_atomic_add v4, v3, s[100:101] offset:2304
	global_atomic_add v4, v3, s[100:101] offset:2560
	global_atomic_add v4, v3, s[100:101] offset:2816
	global_atomic_add v4, v3, s[100:101] offset:3072
	global_atomic_add v4, v3, s[100:101] offset:3328
	global_atomic_add v4, v3, s[100:101] offset:3584
	global_atomic_add v4, v3, s[100:101] offset:3840
.Lgb_poll_0:
	global_load_dword v11, v6, s[100:101] sc1
	v_add_u32_e32 v10, 1, v10
	s_waitcnt vmcnt(0)
	v_cmp_ge_u32_e32 vcc, v11, v9
	s_cbranch_vccnz .Lgb_done_0
	v_cmp_gt_u32_e32 vcc, 0x80000, v10
	s_sleep 1
	s_cbranch_vccnz .Lgb_poll_0
.Lgb_done_0:
	s_waitcnt lgkmcnt(0)
.LBB0_283:
	s_or_b64 exec, exec, s[0:1]
	s_waitcnt lgkmcnt(0)
	s_barrier

.LBB0_306:
	s_cmp_gt_i32 s81, 2
	s_cselect_b64 s[4:5], -1, 0
	s_and_b64 s[0:1], s[0:1], s[4:5]
	s_andn2_b64 vcc, exec, s[0:1]
	s_cbranch_vccnz .LBB0_360
	s_waitcnt vmcnt(0)
	s_waitcnt vmcnt(0)
	s_barrier
	s_and_saveexec_b64 s[0:1], s[78:79]
	s_cbranch_execz .LBB0_359
	v_mov_b32_e32 v1, 0x22160
	s_waitcnt vmcnt(0) lgkmcnt(0)
	ds_read_b32 v2, v1
	v_mov_b32_e32 v3, 1
	v_mov_b32_e32 v4, s99
	v_and_b32_e32 v5, 0xffff, v4
	v_lshrrev_b32_e32 v6, 16, v4
	global_atomic_add v7, v5, v3, s[100:101] sc0
	buffer_inv sc1
	v_lshrrev_b32_e32 v8, 8, v5
	v_sub_u32_e32 v8, s98, v8
	v_add_u32_e32 v8, 7, v8
	v_lshrrev_b32_e32 v8, 3, v8
	v_mov_b32_e32 v9, s98
	v_min_u32_e32 v9, 8, v9
	v_mov_b32_e32 v10, 0
	s_waitcnt lgkmcnt(0)
	v_add_u32_e32 v2, 1, v2
	ds_write_b32 v1, v2
	v_mul_lo_u32 v8, v8, v2
	v_mul_lo_u32 v9, v9, v2
	s_waitcnt vmcnt(0)
	v_add_u32_e32 v7, 1, v7
	v_cmp_eq_u32_e32 vcc, v7, v8
	s_cbranch_vccz .Lgb_poll_1
	v_mov_b32_e32 v4, 0
	global_atomic_add v4, v3, s[100:101] offset:2048
	global_atomic_add v4, v3, s[100:101] offset:2304
	global_atomic_add v4, v3, s[100:101] offset:2560
	global_atomic_add v4, v3, s[100:101] offset:2816
	global_atomic_add v4, v3, s[100:101] offset:3072
	global_atomic_add v4, v3, s[100:101] offset:3328
	global_atomic_add v4, v3, s[100:101] offset:3584
	global_atomic_add v4, v3, s[100:101] offset:3840

.Lgb_done_1:
	s_waitcnt lgkmcnt(0)
.LBB0_359:
	s_or_b64 exec, exec, s[0:1]
	s_waitcnt lgkmcnt(0)
	s_barrier

.LBB0_427:
	s_cmp_gt_i32 s81, 3
	s_cselect_b64 s[4:5], -1, 0
	s_and_b64 s[6:7], s[36:37], s[4:5]
	s_andn2_b64 vcc, exec, s[6:7]
	s_cbranch_vccnz .LBB0_481
	s_waitcnt vmcnt(0)
	s_waitcnt vmcnt(0)
	s_barrier
	s_and_saveexec_b64 s[6:7], s[78:79]
	s_cbranch_execz .LBB0_480
	v_mov_b32_e32 v1, 0x22160
	s_waitcnt vmcnt(0) lgkmcnt(0)
	ds_read_b32 v2, v1
	v_mov_b32_e32 v3, 1
	v_mov_b32_e32 v4, s99
	v_and_b32_e32 v5, 0xffff, v4
	v_lshrrev_b32_e32 v6, 16, v4
	global_atomic_add v7, v5, v3, s[100:101] sc0
	buffer_inv sc1
	v_lshrrev_b32_e32 v8, 8, v5
	v_sub_u32_e32 v8, s98, v8
	v_add_u32_e32 v8, 7, v8
	v_lshrrev_b32_e32 v8, 3, v8
	v_mov_b32_e32 v9, s98
	v_min_u32_e32 v9, 8, v9
	v_mov_b32_e32 v10, 0
	s_waitcnt lgkmcnt(0)
	v_add_u32_e32 v2, 1, v2
	ds_write_b32 v1, v2
	v_mul_lo_u32 v8, v8, v2
	v_mul_lo_u32 v9, v9, v2
	s_waitcnt vmcnt(0)
	v_add_u32_e32 v7, 1, v7
	v_cmp_eq_u32_e32 vcc, v7, v8
	s_cbranch_vccz .Lgb_poll_2
	v_mov_b32_e32 v4, 0
	global_atomic_add v4, v3, s[100:101] offset:2048
	global_atomic_add v4, v3, s[100:101] offset:2304
	global_atomic_add v4, v3, s[100:101] offset:2560
	global_atomic_add v4, v3, s[100:101] offset:2816
	global_atomic_add v4, v3, s[100:101] offset:3072
	global_atomic_add v4, v3, s[100:101] offset:3328
	global_atomic_add v4, v3, s[100:101] offset:3584
	global_atomic_add v4, v3, s[100:101] offset:3840

.Lgb_done_2:
	s_waitcnt lgkmcnt(0)
.LBB0_480:
	s_or_b64 exec, exec, s[6:7]
	s_waitcnt lgkmcnt(0)
	s_barrier

.LBB0_601:
	s_andn2_b64 vcc, exec, s[10:11]
	s_mov_b32 s46, s9
	s_cbranch_vccnz .LBB0_655
	s_waitcnt vmcnt(0)
	s_barrier
	s_mov_b64 s[10:11], exec
	v_readlane_b32 s44, v254, 12
	v_readlane_b32 s45, v254, 13
	s_and_b64 s[44:45], s[10:11], s[44:45]
	s_mov_b64 exec, s[44:45]
	s_cbranch_execz .LBB0_654
	v_mov_b32_e32 v7, 0x22160
	s_waitcnt vmcnt(0) lgkmcnt(0)
	ds_read_b32 v8, v7
	v_mov_b32_e32 v9, 1
	v_mov_b32_e32 v10, s99
	v_and_b32_e32 v11, 0xffff, v10
	v_lshrrev_b32_e32 v12, 16, v10
	global_atomic_add v13, v11, v9, s[100:101] sc0
	buffer_inv sc1
	v_lshrrev_b32_e32 v14, 8, v11
	v_sub_u32_e32 v14, s98, v14
	v_add_u32_e32 v14, 7, v14
	v_lshrrev_b32_e32 v14, 3, v14
	v_mov_b32_e32 v15, s98
	v_min_u32_e32 v15, 8, v15
	v_mov_b32_e32 v16, 0
	s_waitcnt lgkmcnt(0)
	v_add_u32_e32 v8, 1, v8
	ds_write_b32 v7, v8
	v_mul_lo_u32 v14, v14, v8
	v_mul_lo_u32 v15, v15, v8
	s_waitcnt vmcnt(0)
	v_add_u32_e32 v13, 1, v13
	v_cmp_eq_u32_e32 vcc, v13, v14
	s_cbranch_vccz .Lgb_poll_3
	v_mov_b32_e32 v10, 0
	global_atomic_add v10, v9, s[100:101] offset:2048
	global_atomic_add v10, v9, s[100:101] offset:2304
	global_atomic_add v10, v9, s[100:101] offset:2560
	global_atomic_add v10, v9, s[100:101] offset:2816
	global_atomic_add v10, v9, s[100:101] offset:3072
	global_atomic_add v10, v9, s[100:101] offset:3328
	global_atomic_add v10, v9, s[100:101] offset:3584
	global_atomic_add v10, v9, s[100:101] offset:3840
.Lgb_poll_3:
	global_load_dword v17, v12, s[100:101] sc1
	v_add_u32_e32 v16, 1, v16
	s_waitcnt vmcnt(0)
	v_cmp_ge_u32_e32 vcc, v17, v15
	s_cbranch_vccnz .Lgb_done_3
	v_cmp_gt_u32_e32 vcc, 0x80000, v16
	s_sleep 1
	s_cbranch_vccnz .Lgb_poll_3
.Lgb_done_3:
	s_waitcnt lgkmcnt(0)
.LBB0_654:
	s_or_b64 exec, exec, s[10:11]
	v_readlane_b32 s46, v254, 17
	s_waitcnt lgkmcnt(0)
	s_barrier

.LBB0_759:
	s_cmp_gt_i32 s81, 4
	s_cselect_b64 s[0:1], -1, 0
	s_and_b64 s[4:5], s[4:5], s[0:1]
	s_andn2_b64 vcc, exec, s[4:5]
	s_cbranch_vccnz .LBB0_813
	s_waitcnt vmcnt(0)
	s_waitcnt vmcnt(0)
	s_barrier
	s_and_saveexec_b64 s[4:5], s[78:79]
	s_cbranch_execz .LBB0_812
	v_mov_b32_e32 v1, 0x22160
	s_waitcnt vmcnt(0) lgkmcnt(0)
	ds_read_b32 v2, v1
	v_mov_b32_e32 v3, 1
	v_mov_b32_e32 v4, s99
	v_and_b32_e32 v5, 0xffff, v4
	v_lshrrev_b32_e32 v6, 16, v4
	global_atomic_add v7, v5, v3, s[100:101] sc0
	buffer_inv sc1
	v_lshrrev_b32_e32 v8, 8, v5
	v_sub_u32_e32 v8, s98, v8
	v_add_u32_e32 v8, 7, v8
	v_lshrrev_b32_e32 v8, 3, v8
	v_mov_b32_e32 v9, s98
	v_min_u32_e32 v9, 8, v9
	v_mov_b32_e32 v10, 0
	s_waitcnt lgkmcnt(0)
	v_add_u32_e32 v2, 1, v2
	ds_write_b32 v1, v2
	v_mul_lo_u32 v8, v8, v2
	v_mul_lo_u32 v9, v9, v2
	s_waitcnt vmcnt(0)
	v_add_u32_e32 v7, 1, v7
	v_cmp_eq_u32_e32 vcc, v7, v8
	s_cbranch_vccz .Lgb_poll_4
	v_mov_b32_e32 v4, 0
	global_atomic_add v4, v3, s[100:101] offset:2048
	global_atomic_add v4, v3, s[100:101] offset:2304
	global_atomic_add v4, v3, s[100:101] offset:2560
	global_atomic_add v4, v3, s[100:101] offset:2816
	global_atomic_add v4, v3, s[100:101] offset:3072
	global_atomic_add v4, v3, s[100:101] offset:3328
	global_atomic_add v4, v3, s[100:101] offset:3584
	global_atomic_add v4, v3, s[100:101] offset:3840

.Lgb_done_4:
	s_waitcnt lgkmcnt(0)
.LBB0_812:
	s_or_b64 exec, exec, s[4:5]
	s_waitcnt lgkmcnt(0)
	s_barrier

.LBB0_843:
	s_cmp_gt_i32 s81, 5
	s_cselect_b64 s[4:5], -1, 0
	s_and_b64 s[0:1], s[0:1], s[4:5]
	s_andn2_b64 vcc, exec, s[0:1]
	s_cbranch_vccnz .LBB0_897
	s_waitcnt vmcnt(0)
	s_waitcnt vmcnt(0)
	s_barrier
	s_and_saveexec_b64 s[0:1], s[78:79]
	s_cbranch_execz .LBB0_896
	v_mov_b32_e32 v1, 0x22160
	s_waitcnt vmcnt(0) lgkmcnt(0)
	ds_read_b32 v2, v1
	v_mov_b32_e32 v3, 1
	v_mov_b32_e32 v4, s99
	v_and_b32_e32 v5, 0xffff, v4
	v_lshrrev_b32_e32 v6, 16, v4
	global_atomic_add v7, v5, v3, s[100:101] sc0
	buffer_inv sc1
	v_lshrrev_b32_e32 v8, 8, v5
	v_sub_u32_e32 v8, s98, v8
	v_add_u32_e32 v8, 7, v8
	v_lshrrev_b32_e32 v8, 3, v8
	v_mov_b32_e32 v9, s98
	v_min_u32_e32 v9, 8, v9
	v_mov_b32_e32 v10, 0
	s_waitcnt lgkmcnt(0)
	v_add_u32_e32 v2, 1, v2
	ds_write_b32 v1, v2
	v_mul_lo_u32 v8, v8, v2
	v_mul_lo_u32 v9, v9, v2
	s_waitcnt vmcnt(0)
	v_add_u32_e32 v7, 1, v7
	v_cmp_eq_u32_e32 vcc, v7, v8
	s_cbranch_vccz .Lgb_poll_5
	v_mov_b32_e32 v4, 0
	global_atomic_add v4, v3, s[100:101] offset:2048
	global_atomic_add v4, v3, s[100:101] offset:2304
	global_atomic_add v4, v3, s[100:101] offset:2560
	global_atomic_add v4, v3, s[100:101] offset:2816
	global_atomic_add v4, v3, s[100:101] offset:3072
	global_atomic_add v4, v3, s[100:101] offset:3328
	global_atomic_add v4, v3, s[100:101] offset:3584
	global_atomic_add v4, v3, s[100:101] offset:3840

.Lgb_done_5:
	s_waitcnt lgkmcnt(0)
.LBB0_896:
	s_or_b64 exec, exec, s[0:1]
	s_waitcnt lgkmcnt(0)
	s_barrier

.LBB0_944:
	s_cmp_gt_i32 s81, 6
	s_cselect_b64 s[4:5], -1, 0
	s_and_b64 s[0:1], s[0:1], s[4:5]
	s_andn2_b64 vcc, exec, s[0:1]
	s_cbranch_vccnz .LBB0_998
	s_waitcnt vmcnt(0)
	s_waitcnt vmcnt(0)
	s_barrier
	s_and_saveexec_b64 s[0:1], s[78:79]
	s_cbranch_execz .LBB0_997
	v_mov_b32_e32 v1, 0x22160
	s_waitcnt vmcnt(0) lgkmcnt(0)
	ds_read_b32 v2, v1
	v_mov_b32_e32 v3, 1
	v_mov_b32_e32 v4, s99
	v_and_b32_e32 v5, 0xffff, v4
	v_lshrrev_b32_e32 v6, 16, v4
	global_atomic_add v7, v5, v3, s[100:101] sc0
	buffer_inv sc1
	v_lshrrev_b32_e32 v8, 8, v5
	v_sub_u32_e32 v8, s98, v8
	v_add_u32_e32 v8, 7, v8
	v_lshrrev_b32_e32 v8, 3, v8
	v_mov_b32_e32 v9, s98
	v_min_u32_e32 v9, 8, v9
	v_mov_b32_e32 v10, 0
	s_waitcnt lgkmcnt(0)
	v_add_u32_e32 v2, 1, v2
	ds_write_b32 v1, v2
	v_mul_lo_u32 v8, v8, v2
	v_mul_lo_u32 v9, v9, v2
	s_waitcnt vmcnt(0)
	v_add_u32_e32 v7, 1, v7
	v_cmp_eq_u32_e32 vcc, v7, v8
	s_cbranch_vccz .Lgb_poll_6
	v_mov_b32_e32 v4, 0
	global_atomic_add v4, v3, s[100:101] offset:2048
	global_atomic_add v4, v3, s[100:101] offset:2304
	global_atomic_add v4, v3, s[100:101] offset:2560
	global_atomic_add v4, v3, s[100:101] offset:2816
	global_atomic_add v4, v3, s[100:101] offset:3072
	global_atomic_add v4, v3, s[100:101] offset:3328
	global_atomic_add v4, v3, s[100:101] offset:3584
	global_atomic_add v4, v3, s[100:101] offset:3840

.Lgb_done_6:
	s_waitcnt lgkmcnt(0)
.LBB0_997:
	s_or_b64 exec, exec, s[0:1]
	s_waitcnt lgkmcnt(0)
	s_barrier

.LBB0_1151:
	s_cmp_gt_i32 s81, 7
	s_cselect_b64 s[4:5], -1, 0
	s_and_b64 s[0:1], s[76:77], s[4:5]
	v_readlane_b32 s86, v253, 40
	s_andn2_b64 vcc, exec, s[0:1]
	v_readlane_b32 s76, v253, 62
	v_readlane_b32 s77, v253, 63
	v_readlane_b32 s87, v253, 41
	s_cbranch_vccnz .LBB0_1205
	s_waitcnt vmcnt(0)
	s_waitcnt vmcnt(0) lgkmcnt(0)
	s_barrier
	s_and_saveexec_b64 s[0:1], s[78:79]
	s_cbranch_execz .LBB0_1204
	v_mov_b32_e32 v1, 0x22160
	s_waitcnt vmcnt(0) lgkmcnt(0)
	ds_read_b32 v2, v1
	v_mov_b32_e32 v3, 1
	v_mov_b32_e32 v4, s99
	v_and_b32_e32 v5, 0xffff, v4
	v_lshrrev_b32_e32 v6, 16, v4
	global_atomic_add v7, v5, v3, s[100:101] sc0
	buffer_inv sc1
	v_lshrrev_b32_e32 v8, 8, v5
	v_sub_u32_e32 v8, s98, v8
	v_add_u32_e32 v8, 7, v8
	v_lshrrev_b32_e32 v8, 3, v8
	v_mov_b32_e32 v9, s98
	v_min_u32_e32 v9, 8, v9
	v_mov_b32_e32 v10, 0
	s_waitcnt lgkmcnt(0)
	v_add_u32_e32 v2, 1, v2
	ds_write_b32 v1, v2
	v_mul_lo_u32 v8, v8, v2
	v_mul_lo_u32 v9, v9, v2
	s_waitcnt vmcnt(0)
	v_add_u32_e32 v7, 1, v7
	v_cmp_eq_u32_e32 vcc, v7, v8
	s_cbranch_vccz .Lgb_poll_7
	v_mov_b32_e32 v4, 0
	global_atomic_add v4, v3, s[100:101] offset:2048
	global_atomic_add v4, v3, s[100:101] offset:2304
	global_atomic_add v4, v3, s[100:101] offset:2560
	global_atomic_add v4, v3, s[100:101] offset:2816
	global_atomic_add v4, v3, s[100:101] offset:3072
	global_atomic_add v4, v3, s[100:101] offset:3328
	global_atomic_add v4, v3, s[100:101] offset:3584
	global_atomic_add v4, v3, s[100:101] offset:3840

.Lgb_done_7:
	s_waitcnt lgkmcnt(0)
.LBB0_1204:
	s_or_b64 exec, exec, s[0:1]
	s_waitcnt lgkmcnt(0)
	s_barrier

.LBB0_1220:
	s_cmp_gt_i32 s81, 8
	s_cselect_b64 s[14:15], -1, 0
	s_and_b64 s[4:5], s[12:13], s[14:15]
	s_andn2_b64 vcc, exec, s[4:5]
	s_cbranch_vccnz .LBB0_1274
	s_waitcnt vmcnt(0)
	s_waitcnt vmcnt(0) lgkmcnt(0)
	s_barrier
	s_and_saveexec_b64 s[4:5], s[78:79]
	s_cbranch_execz .LBB0_1273
	v_mov_b32_e32 v1, 0x22160
	s_waitcnt vmcnt(0) lgkmcnt(0)
	ds_read_b32 v2, v1
	v_mov_b32_e32 v3, 1
	v_mov_b32_e32 v4, s99
	v_and_b32_e32 v5, 0xffff, v4
	v_lshrrev_b32_e32 v6, 16, v4
	global_atomic_add v7, v5, v3, s[100:101] sc0
	buffer_inv sc1
	v_lshrrev_b32_e32 v8, 8, v5
	v_sub_u32_e32 v8, s98, v8
	v_add_u32_e32 v8, 7, v8
	v_lshrrev_b32_e32 v8, 3, v8
	v_mov_b32_e32 v9, s98
	v_min_u32_e32 v9, 8, v9
	v_mov_b32_e32 v10, 0
	s_waitcnt lgkmcnt(0)
	v_add_u32_e32 v2, 1, v2
	ds_write_b32 v1, v2
	v_mul_lo_u32 v8, v8, v2
	v_mul_lo_u32 v9, v9, v2
	s_waitcnt vmcnt(0)
	v_add_u32_e32 v7, 1, v7
	v_cmp_eq_u32_e32 vcc, v7, v8
	s_cbranch_vccz .Lgb_poll_8
	v_mov_b32_e32 v4, 0
	global_atomic_add v4, v3, s[100:101] offset:2048
	global_atomic_add v4, v3, s[100:101] offset:2304
	global_atomic_add v4, v3, s[100:101] offset:2560
	global_atomic_add v4, v3, s[100:101] offset:2816
	global_atomic_add v4, v3, s[100:101] offset:3072
	global_atomic_add v4, v3, s[100:101] offset:3328
	global_atomic_add v4, v3, s[100:101] offset:3584
	global_atomic_add v4, v3, s[100:101] offset:3840

.Lgb_done_8:
	s_waitcnt lgkmcnt(0)
.LBB0_1273:
	s_or_b64 exec, exec, s[4:5]
	s_waitcnt lgkmcnt(0)
	s_barrier

.LBB0_1606:
	s_cmp_gt_i32 s81, 10
	s_cselect_b64 s[0:1], -1, 0
	s_and_b64 s[4:5], s[12:13], s[0:1]
	s_andn2_b64 vcc, exec, s[4:5]
	s_waitcnt vmcnt(0)
	v_and_b32_e32 v82, 63, v0
	s_cbranch_vccnz .LBB0_1660
	s_waitcnt vmcnt(0)
	s_waitcnt lgkmcnt(0)
	s_barrier
	s_and_saveexec_b64 s[4:5], s[78:79]
	s_cbranch_execz .LBB0_1659
	v_mov_b32_e32 v1, 0x22160
	s_waitcnt vmcnt(0) lgkmcnt(0)
	ds_read_b32 v2, v1
	v_mov_b32_e32 v3, 1
	v_mov_b32_e32 v4, s99
	v_and_b32_e32 v5, 0xffff, v4
	v_lshrrev_b32_e32 v6, 16, v4
	global_atomic_add v7, v5, v3, s[100:101] sc0
	buffer_inv sc1
	v_lshrrev_b32_e32 v8, 8, v5
	v_sub_u32_e32 v8, s98, v8
	v_add_u32_e32 v8, 7, v8
	v_lshrrev_b32_e32 v8, 3, v8
	v_mov_b32_e32 v9, s98
	v_min_u32_e32 v9, 8, v9
	v_mov_b32_e32 v10, 0
	s_waitcnt lgkmcnt(0)
	v_add_u32_e32 v2, 1, v2
	ds_write_b32 v1, v2
	v_mul_lo_u32 v8, v8, v2
	v_mul_lo_u32 v9, v9, v2
	s_waitcnt vmcnt(0)
	v_add_u32_e32 v7, 1, v7
	v_cmp_eq_u32_e32 vcc, v7, v8
	s_cbranch_vccz .Lgb_poll_9
	v_mov_b32_e32 v4, 0
	global_atomic_add v4, v3, s[100:101] offset:2048
	global_atomic_add v4, v3, s[100:101] offset:2304
	global_atomic_add v4, v3, s[100:101] offset:2560
	global_atomic_add v4, v3, s[100:101] offset:2816
	global_atomic_add v4, v3, s[100:101] offset:3072
	global_atomic_add v4, v3, s[100:101] offset:3328
	global_atomic_add v4, v3, s[100:101] offset:3584
	global_atomic_add v4, v3, s[100:101] offset:3840

.Lgb_done_9:
	s_waitcnt lgkmcnt(0)
.LBB0_1659:
	s_or_b64 exec, exec, s[4:5]
	s_waitcnt lgkmcnt(0)
	s_barrier

.LBB0_1750:
	s_waitcnt vmcnt(0)
	s_waitcnt lgkmcnt(0)
	s_barrier
	s_mov_b64 s[6:7], exec
	v_readlane_b32 s40, v253, 46
	s_and_b64 s[8:9], s[6:7], s[78:79]
	v_readlane_b32 s41, v253, 47
	v_readlane_b32 s42, v253, 48
	v_readlane_b32 s43, v253, 49
	v_readlane_b32 s44, v253, 50
	v_readlane_b32 s45, v253, 51
	v_readlane_b32 s52, v253, 58
	v_readlane_b32 s53, v253, 59
	v_readlane_b32 s54, v253, 60
	v_readlane_b32 s55, v253, 61
	v_and_b32_e32 v82, 63, v0
	v_readlane_b32 s46, v253, 52
	v_readlane_b32 s47, v253, 53
	v_readlane_b32 s48, v253, 54
	v_readlane_b32 s49, v253, 55
	v_readlane_b32 s50, v253, 56
	v_readlane_b32 s51, v253, 57
	s_mov_b64 exec, s[8:9]
	s_cbranch_execz .LBB0_1802
	v_mov_b32_e32 v2, 0x22160
	s_waitcnt vmcnt(0) lgkmcnt(0)
	ds_read_b32 v3, v2
	v_mov_b32_e32 v4, 1
	v_mov_b32_e32 v5, s99
	v_and_b32_e32 v6, 0xffff, v5
	v_lshrrev_b32_e32 v7, 16, v5
	global_atomic_add v8, v6, v4, s[100:101] sc0
	buffer_inv sc1
	v_lshrrev_b32_e32 v9, 8, v6
	v_sub_u32_e32 v9, s98, v9
	v_add_u32_e32 v9, 7, v9
	v_lshrrev_b32_e32 v9, 3, v9
	v_mov_b32_e32 v10, s98
	v_min_u32_e32 v10, 8, v10
	v_mov_b32_e32 v11, 0
	s_waitcnt lgkmcnt(0)
	v_add_u32_e32 v3, 1, v3
	ds_write_b32 v2, v3
	v_mul_lo_u32 v9, v9, v3
	v_mul_lo_u32 v10, v10, v3
	s_waitcnt vmcnt(0)
	v_add_u32_e32 v8, 1, v8
	v_cmp_eq_u32_e32 vcc, v8, v9
	s_cbranch_vccz .Lgb_poll_10
	v_mov_b32_e32 v5, 0
	global_atomic_add v5, v4, s[100:101] offset:2048
	global_atomic_add v5, v4, s[100:101] offset:2304
	global_atomic_add v5, v4, s[100:101] offset:2560
	global_atomic_add v5, v4, s[100:101] offset:2816
	global_atomic_add v5, v4, s[100:101] offset:3072
	global_atomic_add v5, v4, s[100:101] offset:3328
	global_atomic_add v5, v4, s[100:101] offset:3584
	global_atomic_add v5, v4, s[100:101] offset:3840
.Lgb_poll_10:
	global_load_dword v12, v7, s[100:101] sc1
	v_add_u32_e32 v11, 1, v11
	s_waitcnt vmcnt(0)
	v_cmp_ge_u32_e32 vcc, v12, v10
	s_cbranch_vccnz .Lgb_done_10
	v_cmp_gt_u32_e32 vcc, 0x80000, v11
	s_sleep 1
	s_cbranch_vccnz .Lgb_poll_10
.Lgb_done_10:
	s_waitcnt lgkmcnt(0)
.LBB0_1802:
	s_or_b64 exec, exec, s[6:7]
	s_waitcnt lgkmcnt(0)
	v_not_b32_e32 v2, 64
	v_lshl_add_u32 v2, v205, 2, v2
	v_add_u32_e32 v3, 0x1f100, v223
	s_mov_b64 s[6:7], 0
	s_movk_i32 s10, 0x100
	s_movk_i32 s11, 0x1ff
	v_mov_b32_e32 v4, v0
	s_barrier
	s_branch .LBB0_1804

.LBB0_1811:
	s_cmp_gt_i32 s81, 11
	s_cselect_b64 s[4:5], -1, 0
	s_and_b64 s[0:1], s[0:1], s[4:5]
	v_readlane_b32 s36, v253, 46
	s_andn2_b64 vcc, exec, s[0:1]
	v_readlane_b32 s37, v253, 47
	v_readlane_b32 s38, v253, 48
	v_readlane_b32 s39, v253, 49
	v_readlane_b32 s40, v253, 50
	v_readlane_b32 s41, v253, 51
	v_readlane_b32 s48, v253, 58
	v_readlane_b32 s49, v253, 59
	v_readlane_b32 s50, v253, 60
	v_readlane_b32 s51, v253, 61
	v_readlane_b32 s42, v253, 52
	v_readlane_b32 s43, v253, 53
	v_readlane_b32 s44, v253, 54
	v_readlane_b32 s45, v253, 55
	v_readlane_b32 s46, v253, 56
	v_readlane_b32 s47, v253, 57
	s_cbranch_vccnz .LBB0_1865
	s_waitcnt vmcnt(0)
	s_waitcnt lgkmcnt(0)
	s_barrier
	s_and_saveexec_b64 s[0:1], s[78:79]
	s_cbranch_execz .LBB0_1864
	v_mov_b32_e32 v1, 0x22160
	s_waitcnt vmcnt(0) lgkmcnt(0)
	ds_read_b32 v2, v1
	v_mov_b32_e32 v3, 1
	v_mov_b32_e32 v4, s99
	v_and_b32_e32 v5, 0xffff, v4
	v_lshrrev_b32_e32 v6, 16, v4
	global_atomic_add v7, v5, v3, s[100:101] sc0
	buffer_inv sc1
	v_lshrrev_b32_e32 v8, 8, v5
	v_sub_u32_e32 v8, s98, v8
	v_add_u32_e32 v8, 7, v8
	v_lshrrev_b32_e32 v8, 3, v8
	v_mov_b32_e32 v9, s98
	v_min_u32_e32 v9, 8, v9
	v_mov_b32_e32 v10, 0
	s_waitcnt lgkmcnt(0)
	v_add_u32_e32 v2, 1, v2
	ds_write_b32 v1, v2
	v_mul_lo_u32 v8, v8, v2
	v_mul_lo_u32 v9, v9, v2
	s_waitcnt vmcnt(0)
	v_add_u32_e32 v7, 1, v7
	v_cmp_eq_u32_e32 vcc, v7, v8
	s_cbranch_vccz .Lgb_poll_11
	v_mov_b32_e32 v4, 0
	global_atomic_add v4, v3, s[100:101] offset:2048
	global_atomic_add v4, v3, s[100:101] offset:2304
	global_atomic_add v4, v3, s[100:101] offset:2560
	global_atomic_add v4, v3, s[100:101] offset:2816
	global_atomic_add v4, v3, s[100:101] offset:3072
	global_atomic_add v4, v3, s[100:101] offset:3328
	global_atomic_add v4, v3, s[100:101] offset:3584
	global_atomic_add v4, v3, s[100:101] offset:3840

.Lgb_done_11:
	s_waitcnt lgkmcnt(0)
.LBB0_1864:
	s_or_b64 exec, exec, s[0:1]
	s_waitcnt lgkmcnt(0)
	s_barrier

.LBB0_1890:
	s_cmp_gt_i32 s81, 12
	s_cselect_b64 s[2:3], -1, 0
	s_and_b64 s[0:1], s[0:1], s[2:3]
	s_andn2_b64 vcc, exec, s[0:1]
	s_cbranch_vccnz .LBB0_1944
	s_waitcnt vmcnt(0)
	s_waitcnt lgkmcnt(0)
	s_barrier
	s_and_saveexec_b64 s[0:1], s[78:79]
	s_cbranch_execz .LBB0_1943
	v_mov_b32_e32 v1, 0x22160
	s_waitcnt vmcnt(0) lgkmcnt(0)
	ds_read_b32 v2, v1
	v_mov_b32_e32 v3, 1
	v_mov_b32_e32 v4, s99
	v_and_b32_e32 v5, 0xffff, v4
	v_lshrrev_b32_e32 v6, 16, v4
	global_atomic_add v7, v5, v3, s[100:101] sc0
	buffer_inv sc1
	v_lshrrev_b32_e32 v8, 8, v5
	v_sub_u32_e32 v8, s98, v8
	v_add_u32_e32 v8, 7, v8
	v_lshrrev_b32_e32 v8, 3, v8
	v_mov_b32_e32 v9, s98
	v_min_u32_e32 v9, 8, v9
	v_mov_b32_e32 v10, 0
	s_waitcnt lgkmcnt(0)
	v_add_u32_e32 v2, 1, v2
	ds_write_b32 v1, v2
	v_mul_lo_u32 v8, v8, v2
	v_mul_lo_u32 v9, v9, v2
	s_waitcnt vmcnt(0)
	v_add_u32_e32 v7, 1, v7
	v_cmp_eq_u32_e32 vcc, v7, v8
	s_cbranch_vccz .Lgb_poll_12
	v_mov_b32_e32 v4, 0
	global_atomic_add v4, v3, s[100:101] offset:2048
	global_atomic_add v4, v3, s[100:101] offset:2304
	global_atomic_add v4, v3, s[100:101] offset:2560
	global_atomic_add v4, v3, s[100:101] offset:2816
	global_atomic_add v4, v3, s[100:101] offset:3072
	global_atomic_add v4, v3, s[100:101] offset:3328
	global_atomic_add v4, v3, s[100:101] offset:3584
	global_atomic_add v4, v3, s[100:101] offset:3840

.Lgb_done_12:
	s_waitcnt lgkmcnt(0)
.LBB0_1943:
	s_or_b64 exec, exec, s[0:1]
	s_waitcnt lgkmcnt(0)
	s_barrier

.LBB0_1991:
	s_cmp_gt_i32 s81, 13
	s_cselect_b64 s[2:3], -1, 0
	s_and_b64 s[0:1], s[0:1], s[2:3]
	s_andn2_b64 vcc, exec, s[0:1]
	s_cbranch_vccnz .LBB0_2045
	s_waitcnt vmcnt(0)
	s_waitcnt lgkmcnt(0)
	s_barrier
	s_and_saveexec_b64 s[0:1], s[78:79]
	s_cbranch_execz .LBB0_2044
	v_mov_b32_e32 v1, 0x22160
	s_waitcnt vmcnt(0) lgkmcnt(0)
	ds_read_b32 v2, v1
	v_mov_b32_e32 v3, 1
	v_mov_b32_e32 v4, s99
	v_and_b32_e32 v5, 0xffff, v4
	v_lshrrev_b32_e32 v6, 16, v4
	global_atomic_add v7, v5, v3, s[100:101] sc0
	buffer_inv sc1
	v_lshrrev_b32_e32 v8, 8, v5
	v_sub_u32_e32 v8, s98, v8
	v_add_u32_e32 v8, 7, v8
	v_lshrrev_b32_e32 v8, 3, v8
	v_mov_b32_e32 v9, s98
	v_min_u32_e32 v9, 8, v9
	v_mov_b32_e32 v10, 0
	s_waitcnt lgkmcnt(0)
	v_add_u32_e32 v2, 1, v2
	ds_write_b32 v1, v2
	v_mul_lo_u32 v8, v8, v2
	v_mul_lo_u32 v9, v9, v2
	s_waitcnt vmcnt(0)
	v_add_u32_e32 v7, 1, v7
	v_cmp_eq_u32_e32 vcc, v7, v8
	s_cbranch_vccz .Lgb_poll_13
	v_mov_b32_e32 v4, 0
	global_atomic_add v4, v3, s[100:101] offset:2048
	global_atomic_add v4, v3, s[100:101] offset:2304
	global_atomic_add v4, v3, s[100:101] offset:2560
	global_atomic_add v4, v3, s[100:101] offset:2816
	global_atomic_add v4, v3, s[100:101] offset:3072
	global_atomic_add v4, v3, s[100:101] offset:3328
	global_atomic_add v4, v3, s[100:101] offset:3584
	global_atomic_add v4, v3, s[100:101] offset:3840

.Lgb_done_13:
	s_waitcnt lgkmcnt(0)
.LBB0_2044:
	s_or_b64 exec, exec, s[0:1]
	s_waitcnt lgkmcnt(0)
	s_barrier

	.amdhsa_kernel _Z9trunk_fwd4Args
		.amdhsa_group_segment_fixed_size 0
		.amdhsa_private_segment_fixed_size 0
		.amdhsa_kernarg_size 464
		.amdhsa_user_sgpr_count 2
		.amdhsa_user_sgpr_dispatch_ptr 0
		.amdhsa_user_sgpr_queue_ptr 0
		.amdhsa_user_sgpr_kernarg_segment_ptr 1
		.amdhsa_user_sgpr_dispatch_id 0
		.amdhsa_user_sgpr_kernarg_preload_length 0
		.amdhsa_user_sgpr_kernarg_preload_offset 0
		.amdhsa_user_sgpr_private_segment_size 0
		.amdhsa_uses_dynamic_stack 0
		.amdhsa_enable_private_segment 0
		.amdhsa_system_sgpr_workgroup_id_x 1
		.amdhsa_system_sgpr_workgroup_id_y 0
		.amdhsa_system_sgpr_workgroup_id_z 0
		.amdhsa_system_sgpr_workgroup_info 0
		.amdhsa_system_vgpr_workitem_id 0
		.amdhsa_next_free_vgpr 256
		.amdhsa_next_free_sgpr 102
		.amdhsa_accum_offset 256
		.amdhsa_reserve_vcc 1
		.amdhsa_float_round_mode_32 0
		.amdhsa_float_round_mode_16_64 0
		.amdhsa_float_denorm_mode_32 3
		.amdhsa_float_denorm_mode_16_64 3
		.amdhsa_dx10_clamp 1
		.amdhsa_ieee_mode 1
		.amdhsa_fp16_overflow 0
		.amdhsa_tg_split 0
		.amdhsa_exception_fp_ieee_invalid_op 0
		.amdhsa_exception_fp_denorm_src 0
		.amdhsa_exception_fp_ieee_div_zero 0
		.amdhsa_exception_fp_ieee_overflow 0
		.amdhsa_exception_fp_ieee_underflow 0
		.amdhsa_exception_fp_ieee_inexact 0
		.amdhsa_exception_int_div_zero 0
	.end_amdhsa_kernel

amdhsa.kernels:
  - .agpr_count:     0
    .args:
      - .offset:         0
        .size:           208
        .value_kind:     by_value
      - .offset:         208
        .size:           4
        .value_kind:     hidden_block_count_x
      - .offset:         212
        .size:           4
        .value_kind:     hidden_block_count_y
      - .offset:         216
        .size:           4
        .value_kind:     hidden_block_count_z
      - .offset:         220
        .size:           2
        .value_kind:     hidden_group_size_x
      - .offset:         222
        .size:           2
        .value_kind:     hidden_group_size_y
      - .offset:         224
        .size:           2
        .value_kind:     hidden_group_size_z
      - .offset:         226
        .size:           2
        .value_kind:     hidden_remainder_x
      - .offset:         228
        .size:           2
        .value_kind:     hidden_remainder_y
      - .offset:         230
        .size:           2
        .value_kind:     hidden_remainder_z
      - .offset:         248
        .size:           8
        .value_kind:     hidden_global_offset_x
      - .offset:         256
        .size:           8
        .value_kind:     hidden_global_offset_y
      - .offset:         264
        .size:           8
        .value_kind:     hidden_global_offset_z
      - .offset:         272
        .size:           2
        .value_kind:     hidden_grid_dims
      - .offset:         328
        .size:           4
        .value_kind:     hidden_dynamic_lds_size
    .group_segment_fixed_size: 0
    .kernarg_segment_align: 8
    .kernarg_segment_size: 464
    .language:       OpenCL C
    .language_version:
      - 2
      - 0
    .max_flat_workgroup_size: 512
    .name:           _Z9trunk_fwd4Args
    .private_segment_fixed_size: 0
    .sgpr_count:     108
    .sgpr_spill_count: 173
    .symbol:         _Z9trunk_fwd4Args.kd
    .uniform_work_group_size: 1
    .uses_dynamic_stack: false
    .vgpr_count:     256
    .vgpr_spill_count: 0
    .wavefront_size: 64
